# v8 + workgroups without a unit in the last MOE1 / MOE2 round start ~6-7 us late (free slack): runs them out of phase with the others
# speedup vs baseline: 1.0076x; 1.0033x over previous
.LBB0_1335:
	s_or_b64 exec, exec, s[0:1]
	s_add_i32 s0, 0, 0x201a0
	v_mov_b32_e32 v6, v0
	v_mov_b32_e32 v1, s0
	s_waitcnt lgkmcnt(0)
	s_barrier
	ds_read_b32 v1, v1
	s_ashr_i32 s2, s94, 3
	s_and_b32 s0, s2, -2
	s_bfe_u32 s3, s94, 0x10002
	s_or_b32 s5, s0, s3
	s_waitcnt lgkmcnt(0)
	v_readlane_b32 s99, v255, 8
	s_nop 0
	s_cmp_lg_u32 s99, 0x100
	s_cbranch_scc1 .Lm1_long
	v_readfirstlane_b32 s99, v1
	s_nop 0
	s_sub_u32 s98, s99, 1
	s_and_b32 s98, s98, 0xffffffe0
	s_lshr_b32 s100, s94, 3
	s_add_i32 s98, s98, s100
	s_and_b32 s98, s98, -2
	s_bfe_u32 s100, s94, 0x10002
	s_add_i32 s98, s98, s100
	s_cmp_lt_i32 s98, s99
	s_cbranch_scc1 .Lm1_long
	s_sleep 127
	s_sleep 60
.Lm1_long:
	v_cmp_ge_i32_e32 vcc, s5, v1
	v_readfirstlane_b32 s4, v6
	v_cmp_lt_i32_e64 s[0:1], s5, v1
	s_cbranch_vccnz .LBB0_1337
	s_add_i32 s10, 0, 0x20160
	v_mov_b32_e32 v1, s10
	ds_read_b32 v1, v1
	s_add_i32 s10, 0, 0x20000
	s_bfe_u32 s11, s94, 0x10003
	s_waitcnt lgkmcnt(0)
	v_cmp_lt_i32_e32 vcc, s5, v1
	s_nop 1
	v_cndmask_b32_e64 v1, 16, 0, vcc
	v_lshlrev_b32_e32 v2, 2, v1
	v_add_u32_e32 v2, s10, v2
	ds_read_b32 v2, v2 offset:320
	s_waitcnt lgkmcnt(0)
	v_cmp_lt_i32_e32 vcc, s5, v2
	s_nop 1
	v_cndmask_b32_e64 v2, 8, 0, vcc
	v_or_b32_e32 v1, v2, v1
	v_lshlrev_b32_e32 v2, 2, v1
	v_add_u32_e32 v2, s10, v2
	ds_read_b32 v2, v2 offset:304
	s_waitcnt lgkmcnt(0)
	v_cmp_lt_i32_e32 vcc, s5, v2
	s_nop 1
	v_cndmask_b32_e64 v2, 4, 0, vcc
	v_or_b32_e32 v1, v2, v1
	v_lshlrev_b32_e32 v2, 2, v1
	v_add_u32_e32 v2, s10, v2
	ds_read_b32 v2, v2 offset:296
	s_waitcnt lgkmcnt(0)
	v_cmp_lt_i32_e32 vcc, s5, v2
	s_nop 1
	v_cndmask_b32_e64 v2, 2, 0, vcc
	v_or_b32_e32 v1, v2, v1
	v_lshlrev_b32_e32 v2, 2, v1
	v_add_u32_e32 v2, s10, v2
	ds_read_b32 v2, v2 offset:292
	s_waitcnt lgkmcnt(0)
	v_cmp_ge_i32_e32 vcc, s5, v2
	s_nop 1
	v_cndmask_b32_e64 v2, 0, 1, vcc
	v_or_b32_e32 v2, v1, v2
	v_lshlrev_b32_e32 v1, 2, v2
	v_add_u32_e32 v1, s10, v1
	ds_read_b32 v3, v1 offset:288
	ds_read2_b32 v[8:9], v1 offset1:32
	s_lshl_b32 s10, s94, 1
	s_and_b32 s10, s10, 6
	s_or_b32 s36, s11, s10
	s_waitcnt lgkmcnt(1)
	v_sub_u32_e32 v1, s5, v3
	v_lshlrev_b32_e32 v5, 8, v1
	s_waitcnt lgkmcnt(0)
	v_sub_u32_e32 v1, v8, v5
	v_min_i32_e32 v226, 0x100, v1
	v_add_u32_e32 v1, v9, v5
	s_andn2_b64 vcc, exec, s[0:1]
	s_cbranch_vccz .LBB0_1338
	s_branch .LBB0_1390

.LBB0_1452:
	s_cmp_lt_i32 s86, 11
	s_cselect_b64 s[6:7], -1, 0
	s_and_b64 s[0:1], s[6:7], s[0:1]
	s_andn2_b64 vcc, exec, s[0:1]
	s_cbranch_vccnz .LBB0_1498
	s_waitcnt vmcnt(0)
	v_mov_b32_e32 v1, v0
	v_mov_b32_e32 v2, 0x201a0
	ds_read_b32 v2, v2
	v_readlane_b32 s99, v255, 8
	s_nop 0
	s_cmp_lg_u32 s99, 0x100
	s_cbranch_scc1 .Lm2_long
	s_waitcnt lgkmcnt(0)
	v_readfirstlane_b32 s99, v2
	s_nop 0
	s_sub_u32 s98, s99, 1
	s_and_b32 s98, s98, 0xffffffe0
	s_lshr_b32 s100, s94, 3
	s_add_i32 s98, s98, s100
	s_and_b32 s98, s98, -2
	s_bfe_u32 s100, s94, 0x10002
	s_add_i32 s98, s98, s100
	s_cmp_lt_i32 s98, s99
	s_cbranch_scc1 .Lm2_long
	s_sleep 127
	s_sleep 100
.Lm2_long:
	s_waitcnt lgkmcnt(0)
	s_load_dwordx2 s[8:9], s[44:45], 0xd8
	s_branch .LBB0_1459
	v_cmp_gt_i32_e32 vcc, 32, v1
	s_and_saveexec_b64 s[0:1], vcc
	s_cbranch_execz .LBB0_1455
	v_lshlrev_b32_e32 v2, 4, v1
	v_ashrrev_i32_e32 v3, 31, v2
	s_waitcnt lgkmcnt(0)
	v_lshl_add_u64 v[2:3], v[2:3], 2, s[8:9]
	v_add_co_u32_e32 v2, vcc, 0x8000, v2
	s_nop 1
	v_addc_co_u32_e32 v3, vcc, 0, v3, vcc
	global_load_dword v2, v[2:3], off sc1
	v_lshl_add_u32 v3, v1, 2, 0
	v_add_u32_e32 v3, 0x20000, v3
	s_waitcnt vmcnt(0)
	ds_write_b32 v3, v2
